# agg1: degree ranks by cooperative counting across the 4 waves (8 readlane compares each, partial counts summed through LDS, ds_permute by rank) instead of a full 32-key bitonic sort in every wave
# baseline (speedup 1.0000x reference)
_Z11agg1_kernelPKDF16_PKfS2_PKiS4_S2_S2_PDF16_PfS6_i:
	s_load_dwordx8 s[4:11], s[0:1], 0x0
	s_load_dwordx8 s[12:19], s[0:1], 0x20
	s_load_dwordx4 s[20:23], s[0:1], 0x40
	s_load_dword s24, s[0:1], 0x50
	v_lshlrev_b32_e32 v32, 2, v0
	v_readfirstlane_b32 s25, v0
	s_lshl_b32 s26, s2, 5
	v_and_b32_e32 v64, 7, v0
	v_bfe_u32 v65, v0, 3, 3
	v_and_b32_e32 v45, 31, v0
	s_lshr_b32 s25, s25, 6
	s_getreg_b32 s30, hwreg(HW_REG_HW_ID, 4, 2)
	s_lshr_b32 s31, s2, 8
	s_lshl_b32 s31, s31, 3
	s_mov_b32 s44, 0x276c9c8d
	s_mov_b32 s45, 0xe46393
	s_and_b32 s47, s2, 0xff
	s_cmp_lt_u32 s47, 27
	s_cselect_b32 s44, 0xb1784b63, s44
	s_cselect_b32 s45, 0x1e4ee4, s45
	s_lshr_b64 s[44:45], s[44:45], s31
	s_lshl_b32 s31, s30, 1
	s_lshr_b32 s44, s44, s31
	s_and_b32 s44, s44, 3
	s_lshl_b32 s45, 1, s30
	s_lshl_b32 s46, s25, 2
	s_addk_i32 s46, 0x2800
	v_mov_b32_e32 v49, s45
	v_mov_b32_e32 v50, s46
	ds_write_b32 v50, v49
	v_lshlrev_b32_e32 v1, 1, v64
	v_add_u32_e32 v46, s26, v45
	s_waitcnt lgkmcnt(0)
	global_load_dword v33, v32, s[14:15]
	global_load_dword v34, v32, s[16:17]
	s_add_i32 s28, s24, -1
	v_cmp_gt_i32_e64 s[38:39], s24, v46
	v_min_i32_e32 v46, s28, v46
	v_lshlrev_b32_e32 v47, 2, v46
	global_load_dword v44, v47, s[10:11]
	global_load_dword v48, v47, s[10:11] offset:4
	s_lshl_b32 s27, s25, 11
	v_lshlrev_b32_e32 v62, 6, v64
	v_add_u32_e32 v62, 0x2000, v62
	v_cmp_eq_u32_e64 s[34:35], 0, v64
	v_lshlrev_b32_e32 v35, 8, v64
	v_lshl_add_u32 v35, v65, 4, v35
	v_add_u32_e32 v63, s27, v35
	v_mov_b32_e32 v36, 0
	v_mov_b32_e32 v37, 0
	v_mov_b32_e32 v38, 0
	v_mov_b32_e32 v39, 0
	s_waitcnt vmcnt(2)
	ds_write2st64_b32 v32, v33, v34 offset0:32 offset1:36
	ds_write_b128 v63, v[36:39]
	ds_write_b128 v63, v[36:39] offset:128
	s_waitcnt vmcnt(0)
	v_sub_u32_e32 v48, v48, v44
	v_add_u32_e32 v48, 1, v48
	v_cndmask_b32_e64 v48, 0, v48, s[38:39]
	v_lshl_or_b32 v40, v48, 5, v45
	s_lshl_b32 s31, s25, 2
	s_addk_i32 s31, 0x2810
	s_lshl_b32 s47, s25, 3
	v_mov_b32_e32 v41, 0
	s_nop 1
	v_readlane_b32 s46, v40, s47
	s_add_i32 s47, s47, 1
	v_cmp_gt_u32_e32 vcc, s46, v40
	v_addc_co_u32_e32 v41, vcc, 0, v41, vcc
	v_readlane_b32 s46, v40, s47
	s_add_i32 s47, s47, 1
	v_cmp_gt_u32_e32 vcc, s46, v40
	v_addc_co_u32_e32 v41, vcc, 0, v41, vcc
	v_readlane_b32 s46, v40, s47
	s_add_i32 s47, s47, 1
	v_cmp_gt_u32_e32 vcc, s46, v40
	v_addc_co_u32_e32 v41, vcc, 0, v41, vcc
	v_readlane_b32 s46, v40, s47
	s_add_i32 s47, s47, 1
	v_cmp_gt_u32_e32 vcc, s46, v40
	v_addc_co_u32_e32 v41, vcc, 0, v41, vcc
	v_readlane_b32 s46, v40, s47
	s_add_i32 s47, s47, 1
	v_cmp_gt_u32_e32 vcc, s46, v40
	v_addc_co_u32_e32 v41, vcc, 0, v41, vcc
	v_readlane_b32 s46, v40, s47
	s_add_i32 s47, s47, 1
	v_cmp_gt_u32_e32 vcc, s46, v40
	v_addc_co_u32_e32 v41, vcc, 0, v41, vcc
	v_readlane_b32 s46, v40, s47
	s_add_i32 s47, s47, 1
	v_cmp_gt_u32_e32 vcc, s46, v40
	v_addc_co_u32_e32 v41, vcc, 0, v41, vcc
	v_readlane_b32 s46, v40, s47
	s_add_i32 s47, s47, 1
	v_cmp_gt_u32_e32 vcc, s46, v40
	v_addc_co_u32_e32 v41, vcc, 0, v41, vcc
	v_lshl_add_u32 v42, v45, 4, s31
	ds_write_b32 v42, v41
	v_mov_b32_e32 v50, 0x2800
	s_waitcnt lgkmcnt(0)
	s_barrier
	ds_read_b128 v[52:55], v50
	v_lshlrev_b32_e32 v42, 4, v45
	ds_read_b128 v[48:51], v42 offset:10256
	s_waitcnt lgkmcnt(1)
	v_or3_b32 v52, v52, v53, v54
	v_or_b32_e32 v52, v52, v55
	s_nop 0
	v_readfirstlane_b32 s46, v52
	s_cmp_eq_u32 s46, 15
	s_cselect_b32 s44, s44, s25
	s_lshl_b32 s40, s44, 3
	s_waitcnt lgkmcnt(0)
	v_add3_u32 v48, v48, v49, v50
	v_add_u32_e32 v48, v48, v51
	v_lshlrev_b32_e32 v48, 2, v48
	ds_permute_b32 v40, v48, v40
	v_add_u32_e32 v45, s40, v65
	v_lshlrev_b32_e32 v45, 2, v45
	s_waitcnt lgkmcnt(0)
	ds_bpermute_b32 v46, v45, v40
	s_waitcnt lgkmcnt(0)
	v_and_b32_e32 v15, 31, v46
	v_lshrrev_b32_e32 v11, 5, v46
	v_lshlrev_b32_e32 v47, 2, v15
	ds_bpermute_b32 v10, v47, v44
	v_add_u32_e32 v66, s26, v15
	v_min_i32_e32 v66, s28, v66
	v_cmp_lt_u32_e64 s[36:37], 0, v11
	v_lshlrev_b32_e32 v4, 2, v66
	v_lshlrev_b32_e32 v35, 2, v64
	v_lshl_or_b32 v35, v66, 5, v35
	global_load_dword v9, v35, s[8:9]
	v_lshrrev_b32_e32 v3, 3, v15
	v_lshlrev_b32_e32 v3, 11, v3
	v_and_b32_e32 v47, 7, v15
	v_lshl_add_u32 v3, v47, 1, v3
	v_lshl_add_u32 v3, v64, 4, v3
	v_readfirstlane_b32 s29, v11
	s_waitcnt lgkmcnt(0)
	v_add_u32_e32 v67, v10, v64
	v_lshlrev_b32_e32 v67, 2, v67
	v_mov_b32_e32 v5, s24
	v_mov_b32_e32 v6, s24
	v_mov_b32_e32 v7, s24
	v_mov_b32_e32 v8, s24
	v_mov_b32_e32 v69, s24
	v_cndmask_b32_e64 v5, v5, v66, s[34:35]
	v_cmp_gt_i32_e32 vcc, v11, v64
	s_andn2_b64 s[40:41], vcc, s[34:35]
	s_and_saveexec_b64 s[32:33], s[40:41]
	global_load_dword v5, v67, s[12:13] offset:-4
	s_mov_b64 exec, s[32:33]
	v_add_u32_e32 v68, 8, v64
	v_cmp_gt_i32_e32 vcc, v11, v68
	s_and_saveexec_b64 s[32:33], vcc
	global_load_dword v6, v67, s[12:13] offset:28
	s_mov_b64 exec, s[32:33]
	v_add_u32_e32 v68, 16, v64
	v_cmp_gt_i32_e32 vcc, v11, v68
	s_and_saveexec_b64 s[32:33], vcc
	global_load_dword v7, v67, s[12:13] offset:60
	s_mov_b64 exec, s[32:33]
	v_add_u32_e32 v68, 24, v64
	v_cmp_gt_i32_e32 vcc, v11, v68
	s_and_saveexec_b64 s[32:33], vcc
	global_load_dword v8, v67, s[12:13] offset:92
	s_mov_b64 exec, s[32:33]
	v_add_u32_e32 v68, 32, v64
	v_cmp_gt_i32_e32 vcc, v11, v68
	s_and_saveexec_b64 s[32:33], vcc
	global_load_dword v69, v67, s[12:13] offset:124
	s_mov_b64 exec, s[32:33]
	s_waitcnt vmcnt(0)
	v_lshlrev_b32_e32 v5, 4, v5
	v_lshlrev_b32_e32 v6, 4, v6
	v_lshlrev_b32_e32 v7, 4, v7
	v_lshlrev_b32_e32 v8, 4, v8
	v_lshlrev_b32_e32 v69, 4, v69
	s_mov_b32 s42, 0
	s_mov_b32 s43, 0
	ds_swizzle_b32 v32, v5 offset:swizzle(BITMASK_PERM, "pp000")
	ds_swizzle_b32 v33, v5 offset:swizzle(BITMASK_PERM, "pp001")
	ds_swizzle_b32 v34, v5 offset:swizzle(BITMASK_PERM, "pp010")
	ds_swizzle_b32 v35, v5 offset:swizzle(BITMASK_PERM, "pp011")
	s_cmp_lt_i32 s29, 3
	s_cbranch_scc1 .Lagg_first_half
	s_waitcnt lgkmcnt(0)
	v_or_b32_e32 v32, v32, v1
	v_or_b32_e32 v33, v33, v1
	v_or_b32_e32 v34, v34, v1
	v_or_b32_e32 v35, v35, v1
	global_load_ushort v36, v32, s[6:7]
	global_load_ushort v37, v33, s[6:7]
	global_load_ushort v38, v34, s[6:7]
	global_load_ushort v39, v35, s[6:7]
	v_lshlrev_b32_e32 v32, 3, v32
	v_lshlrev_b32_e32 v33, 3, v33
	v_lshlrev_b32_e32 v34, 3, v34
	v_lshlrev_b32_e32 v35, 3, v35
	global_load_dwordx4 v[40:43], v32, s[4:5]
	global_load_dwordx4 v[44:47], v33, s[4:5]
	global_load_dwordx4 v[48:51], v34, s[4:5]
	global_load_dwordx4 v[52:55], v35, s[4:5]
	ds_swizzle_b32 v32, v5 offset:swizzle(BITMASK_PERM, "pp100")
	ds_swizzle_b32 v33, v5 offset:swizzle(BITMASK_PERM, "pp101")
	ds_swizzle_b32 v34, v5 offset:swizzle(BITMASK_PERM, "pp110")
	ds_swizzle_b32 v35, v5 offset:swizzle(BITMASK_PERM, "pp111")
	s_waitcnt vmcnt(4)
	v_fma_mix_f32 v36, v36, 1.0, v9 op_sel_hi:[1,0,0]
	v_fma_mix_f32 v37, v37, 1.0, v9 op_sel_hi:[1,0,0]
	v_fma_mix_f32 v38, v38, 1.0, v9 op_sel_hi:[1,0,0]
	v_fma_mix_f32 v39, v39, 1.0, v9 op_sel_hi:[1,0,0]
	v_mul_f32_e32 v58, 0x3e4ccccd, v36
	v_mul_f32_e32 v59, 0x3e4ccccd, v37
	v_mul_f32_e32 v60, 0x3e4ccccd, v38
	v_mul_f32_e32 v61, 0x3e4ccccd, v39
	v_max_f32_e32 v36, v36, v58
	v_max_f32_e32 v37, v37, v59
	v_max_f32_e32 v38, v38, v60
	v_max_f32_e32 v39, v39, v61
	v_max3_f32 v56, v36, v37, v38
	v_max_f32_e32 v13, v56, v39
	v_sub_f32_e32 v36, v36, v13
	v_sub_f32_e32 v37, v37, v13
	v_sub_f32_e32 v38, v38, v13
	v_sub_f32_e32 v39, v39, v13
	v_exp_f32_e32 v36, v36
	v_exp_f32_e32 v37, v37
	v_exp_f32_e32 v38, v38
	v_exp_f32_e32 v39, v39
	s_nop 0
	v_add_f32_e32 v14, v36, v37
	v_add_f32_e32 v14, v14, v38
	v_add_f32_e32 v14, v14, v39
	s_waitcnt vmcnt(3)
	v_cvt_scalef32_pk_f16_fp8 v58, v40, 1.0
	v_cvt_scalef32_pk_f16_fp8 v59, v40, 1.0 op_sel:[1,0,0]
	v_cvt_scalef32_pk_f16_fp8 v60, v41, 1.0
	v_cvt_scalef32_pk_f16_fp8 v61, v41, 1.0 op_sel:[1,0,0]
	v_fma_mix_f32 v16, v58, v36, 0 op_sel_hi:[1,0,0]
	v_fma_mix_f32 v17, v58, v36, 0 op_sel:[1,0,0] op_sel_hi:[1,0,0]
	v_fma_mix_f32 v18, v59, v36, 0 op_sel_hi:[1,0,0]
	v_fma_mix_f32 v19, v59, v36, 0 op_sel:[1,0,0] op_sel_hi:[1,0,0]
	v_fma_mix_f32 v20, v60, v36, 0 op_sel_hi:[1,0,0]
	v_fma_mix_f32 v21, v60, v36, 0 op_sel:[1,0,0] op_sel_hi:[1,0,0]
	v_fma_mix_f32 v22, v61, v36, 0 op_sel_hi:[1,0,0]
	v_fma_mix_f32 v23, v61, v36, 0 op_sel:[1,0,0] op_sel_hi:[1,0,0]
	v_cvt_scalef32_pk_f16_fp8 v58, v42, 1.0
	v_cvt_scalef32_pk_f16_fp8 v59, v42, 1.0 op_sel:[1,0,0]
	v_cvt_scalef32_pk_f16_fp8 v60, v43, 1.0
	v_cvt_scalef32_pk_f16_fp8 v61, v43, 1.0 op_sel:[1,0,0]
	v_fma_mix_f32 v24, v58, v36, 0 op_sel_hi:[1,0,0]
	v_fma_mix_f32 v25, v58, v36, 0 op_sel:[1,0,0] op_sel_hi:[1,0,0]
	v_fma_mix_f32 v26, v59, v36, 0 op_sel_hi:[1,0,0]
	v_fma_mix_f32 v27, v59, v36, 0 op_sel:[1,0,0] op_sel_hi:[1,0,0]
	v_fma_mix_f32 v28, v60, v36, 0 op_sel_hi:[1,0,0]
	v_fma_mix_f32 v29, v60, v36, 0 op_sel:[1,0,0] op_sel_hi:[1,0,0]
	v_fma_mix_f32 v30, v61, v36, 0 op_sel_hi:[1,0,0]
	v_fma_mix_f32 v31, v61, v36, 0 op_sel:[1,0,0] op_sel_hi:[1,0,0]
	s_waitcnt vmcnt(2)
	v_cvt_scalef32_pk_f16_fp8 v58, v44, 1.0
	v_cvt_scalef32_pk_f16_fp8 v59, v44, 1.0 op_sel:[1,0,0]
	v_cvt_scalef32_pk_f16_fp8 v60, v45, 1.0
	v_cvt_scalef32_pk_f16_fp8 v61, v45, 1.0 op_sel:[1,0,0]
	v_fma_mix_f32 v16, v58, v37, v16 op_sel_hi:[1,0,0]
	v_fma_mix_f32 v17, v58, v37, v17 op_sel:[1,0,0] op_sel_hi:[1,0,0]
	v_fma_mix_f32 v18, v59, v37, v18 op_sel_hi:[1,0,0]
	v_fma_mix_f32 v19, v59, v37, v19 op_sel:[1,0,0] op_sel_hi:[1,0,0]
	v_fma_mix_f32 v20, v60, v37, v20 op_sel_hi:[1,0,0]
	v_fma_mix_f32 v21, v60, v37, v21 op_sel:[1,0,0] op_sel_hi:[1,0,0]
	v_fma_mix_f32 v22, v61, v37, v22 op_sel_hi:[1,0,0]
	v_fma_mix_f32 v23, v61, v37, v23 op_sel:[1,0,0] op_sel_hi:[1,0,0]
	v_cvt_scalef32_pk_f16_fp8 v58, v46, 1.0
	v_cvt_scalef32_pk_f16_fp8 v59, v46, 1.0 op_sel:[1,0,0]
	v_cvt_scalef32_pk_f16_fp8 v60, v47, 1.0
	v_cvt_scalef32_pk_f16_fp8 v61, v47, 1.0 op_sel:[1,0,0]
	v_fma_mix_f32 v24, v58, v37, v24 op_sel_hi:[1,0,0]
	v_fma_mix_f32 v25, v58, v37, v25 op_sel:[1,0,0] op_sel_hi:[1,0,0]
	v_fma_mix_f32 v26, v59, v37, v26 op_sel_hi:[1,0,0]
	v_fma_mix_f32 v27, v59, v37, v27 op_sel:[1,0,0] op_sel_hi:[1,0,0]
	v_fma_mix_f32 v28, v60, v37, v28 op_sel_hi:[1,0,0]
	v_fma_mix_f32 v29, v60, v37, v29 op_sel:[1,0,0] op_sel_hi:[1,0,0]
	v_fma_mix_f32 v30, v61, v37, v30 op_sel_hi:[1,0,0]
	v_fma_mix_f32 v31, v61, v37, v31 op_sel:[1,0,0] op_sel_hi:[1,0,0]
	s_waitcnt vmcnt(1)
	v_cvt_scalef32_pk_f16_fp8 v58, v48, 1.0
	v_cvt_scalef32_pk_f16_fp8 v59, v48, 1.0 op_sel:[1,0,0]
	v_cvt_scalef32_pk_f16_fp8 v60, v49, 1.0
	v_cvt_scalef32_pk_f16_fp8 v61, v49, 1.0 op_sel:[1,0,0]
	v_fma_mix_f32 v16, v58, v38, v16 op_sel_hi:[1,0,0]
	v_fma_mix_f32 v17, v58, v38, v17 op_sel:[1,0,0] op_sel_hi:[1,0,0]
	v_fma_mix_f32 v18, v59, v38, v18 op_sel_hi:[1,0,0]
	v_fma_mix_f32 v19, v59, v38, v19 op_sel:[1,0,0] op_sel_hi:[1,0,0]
	v_fma_mix_f32 v20, v60, v38, v20 op_sel_hi:[1,0,0]
	v_fma_mix_f32 v21, v60, v38, v21 op_sel:[1,0,0] op_sel_hi:[1,0,0]
	v_fma_mix_f32 v22, v61, v38, v22 op_sel_hi:[1,0,0]
	v_fma_mix_f32 v23, v61, v38, v23 op_sel:[1,0,0] op_sel_hi:[1,0,0]
	v_cvt_scalef32_pk_f16_fp8 v58, v50, 1.0
	v_cvt_scalef32_pk_f16_fp8 v59, v50, 1.0 op_sel:[1,0,0]
	v_cvt_scalef32_pk_f16_fp8 v60, v51, 1.0
	v_cvt_scalef32_pk_f16_fp8 v61, v51, 1.0 op_sel:[1,0,0]
	v_fma_mix_f32 v24, v58, v38, v24 op_sel_hi:[1,0,0]
	v_fma_mix_f32 v25, v58, v38, v25 op_sel:[1,0,0] op_sel_hi:[1,0,0]
	v_fma_mix_f32 v26, v59, v38, v26 op_sel_hi:[1,0,0]
	v_fma_mix_f32 v27, v59, v38, v27 op_sel:[1,0,0] op_sel_hi:[1,0,0]
	v_fma_mix_f32 v28, v60, v38, v28 op_sel_hi:[1,0,0]
	v_fma_mix_f32 v29, v60, v38, v29 op_sel:[1,0,0] op_sel_hi:[1,0,0]
	v_fma_mix_f32 v30, v61, v38, v30 op_sel_hi:[1,0,0]
	v_fma_mix_f32 v31, v61, v38, v31 op_sel:[1,0,0] op_sel_hi:[1,0,0]
	s_waitcnt vmcnt(0)
	v_cvt_scalef32_pk_f16_fp8 v58, v52, 1.0
	v_cvt_scalef32_pk_f16_fp8 v59, v52, 1.0 op_sel:[1,0,0]
	v_cvt_scalef32_pk_f16_fp8 v60, v53, 1.0
	v_cvt_scalef32_pk_f16_fp8 v61, v53, 1.0 op_sel:[1,0,0]
	v_fma_mix_f32 v16, v58, v39, v16 op_sel_hi:[1,0,0]
	v_fma_mix_f32 v17, v58, v39, v17 op_sel:[1,0,0] op_sel_hi:[1,0,0]
	v_fma_mix_f32 v18, v59, v39, v18 op_sel_hi:[1,0,0]
	v_fma_mix_f32 v19, v59, v39, v19 op_sel:[1,0,0] op_sel_hi:[1,0,0]
	v_fma_mix_f32 v20, v60, v39, v20 op_sel_hi:[1,0,0]
	v_fma_mix_f32 v21, v60, v39, v21 op_sel:[1,0,0] op_sel_hi:[1,0,0]
	v_fma_mix_f32 v22, v61, v39, v22 op_sel_hi:[1,0,0]
	v_fma_mix_f32 v23, v61, v39, v23 op_sel:[1,0,0] op_sel_hi:[1,0,0]
	v_cvt_scalef32_pk_f16_fp8 v58, v54, 1.0
	v_cvt_scalef32_pk_f16_fp8 v59, v54, 1.0 op_sel:[1,0,0]
	v_cvt_scalef32_pk_f16_fp8 v60, v55, 1.0
	v_cvt_scalef32_pk_f16_fp8 v61, v55, 1.0 op_sel:[1,0,0]
	v_fma_mix_f32 v24, v58, v39, v24 op_sel_hi:[1,0,0]
	v_fma_mix_f32 v25, v58, v39, v25 op_sel:[1,0,0] op_sel_hi:[1,0,0]
	v_fma_mix_f32 v26, v59, v39, v26 op_sel_hi:[1,0,0]
	v_fma_mix_f32 v27, v59, v39, v27 op_sel:[1,0,0] op_sel_hi:[1,0,0]
	v_fma_mix_f32 v28, v60, v39, v28 op_sel_hi:[1,0,0]
	v_fma_mix_f32 v29, v60, v39, v29 op_sel:[1,0,0] op_sel_hi:[1,0,0]
	v_fma_mix_f32 v30, v61, v39, v30 op_sel_hi:[1,0,0]
	v_fma_mix_f32 v31, v61, v39, v31 op_sel:[1,0,0] op_sel_hi:[1,0,0]
	s_sub_i32 s29, s29, 4
	s_branch .Lagg_B

	.amdhsa_kernel _Z11agg1_kernelPKDF16_PKfS2_PKiS4_S2_S2_PDF16_PfS6_i
		.amdhsa_group_segment_fixed_size 10768
		.amdhsa_private_segment_fixed_size 0
		.amdhsa_kernarg_size 84
		.amdhsa_user_sgpr_count 2
		.amdhsa_user_sgpr_dispatch_ptr 0
		.amdhsa_user_sgpr_queue_ptr 0
		.amdhsa_user_sgpr_kernarg_segment_ptr 1
		.amdhsa_user_sgpr_dispatch_id 0
		.amdhsa_user_sgpr_kernarg_preload_length 0
		.amdhsa_user_sgpr_kernarg_preload_offset 0
		.amdhsa_user_sgpr_private_segment_size 0
		.amdhsa_uses_dynamic_stack 0
		.amdhsa_enable_private_segment 0
		.amdhsa_system_sgpr_workgroup_id_x 1
		.amdhsa_system_sgpr_workgroup_id_y 0
		.amdhsa_system_sgpr_workgroup_id_z 0
		.amdhsa_system_sgpr_workgroup_info 0
		.amdhsa_system_vgpr_workitem_id 0
		.amdhsa_next_free_vgpr 70
		.amdhsa_next_free_sgpr 48
		.amdhsa_accum_offset 72
		.amdhsa_reserve_vcc 1
		.amdhsa_float_round_mode_32 0
		.amdhsa_float_round_mode_16_64 0
		.amdhsa_float_denorm_mode_32 3
		.amdhsa_float_denorm_mode_16_64 3
		.amdhsa_dx10_clamp 1
		.amdhsa_ieee_mode 1
		.amdhsa_fp16_overflow 0
		.amdhsa_tg_split 0
		.amdhsa_exception_fp_ieee_invalid_op 0
		.amdhsa_exception_fp_denorm_src 0
		.amdhsa_exception_fp_ieee_div_zero 0
		.amdhsa_exception_fp_ieee_overflow 0
		.amdhsa_exception_fp_ieee_underflow 0
		.amdhsa_exception_fp_ieee_inexact 0
		.amdhsa_exception_int_div_zero 0
	.end_amdhsa_kernel

amdhsa.kernels:
  - .agpr_count:     0
    .args:
      - .actual_access:  read_only
        .address_space:  global
        .offset:         0
        .size:           8
        .value_kind:     global_buffer
      - .actual_access:  read_only
        .address_space:  global
        .offset:         8
        .size:           8
        .value_kind:     global_buffer
      - .actual_access:  read_only
        .address_space:  global
        .offset:         16
        .size:           8
        .value_kind:     global_buffer
      - .actual_access:  read_only
        .address_space:  global
        .offset:         24
        .size:           8
        .value_kind:     global_buffer
      - .actual_access:  read_only
        .address_space:  global
        .offset:         32
        .size:           8
        .value_kind:     global_buffer
      - .actual_access:  read_only
        .address_space:  global
        .offset:         40
        .size:           8
        .value_kind:     global_buffer
      - .actual_access:  read_only
        .address_space:  global
        .offset:         48
        .size:           8
        .value_kind:     global_buffer
      - .actual_access:  read_only
        .address_space:  global
        .offset:         56
        .size:           8
        .value_kind:     global_buffer
      - .actual_access:  read_only
        .address_space:  global
        .offset:         64
        .size:           8
        .value_kind:     global_buffer
      - .actual_access:  read_only
        .address_space:  global
        .offset:         72
        .size:           8
        .value_kind:     global_buffer
      - .actual_access:  read_only
        .address_space:  global
        .offset:         80
        .size:           8
        .value_kind:     global_buffer
      - .actual_access:  read_only
        .address_space:  global
        .offset:         88
        .size:           8
        .value_kind:     global_buffer
      - .actual_access:  read_only
        .address_space:  global
        .offset:         96
        .size:           8
        .value_kind:     global_buffer
      - .actual_access:  write_only
        .address_space:  global
        .offset:         104
        .size:           8
        .value_kind:     global_buffer
      - .actual_access:  write_only
        .address_space:  global
        .offset:         112
        .size:           8
        .value_kind:     global_buffer
      - .actual_access:  write_only
        .address_space:  global
        .offset:         120
        .size:           8
        .value_kind:     global_buffer
      - .actual_access:  write_only
        .address_space:  global
        .offset:         128
        .size:           8
        .value_kind:     global_buffer
      - .actual_access:  write_only
        .address_space:  global
        .offset:         136
        .size:           8
        .value_kind:     global_buffer
      - .actual_access:  write_only
        .address_space:  global
        .offset:         144
        .size:           8
        .value_kind:     global_buffer
      - .actual_access:  write_only
        .address_space:  global
        .offset:         152
        .size:           8
        .value_kind:     global_buffer
      - .actual_access:  write_only
        .address_space:  global
        .offset:         160
        .size:           8
        .value_kind:     global_buffer
      - .actual_access:  write_only
        .address_space:  global
        .offset:         168
        .size:           8
        .value_kind:     global_buffer
      - .actual_access:  read_only
        .address_space:  global
        .offset:         176
        .size:           8
        .value_kind:     global_buffer
    .group_segment_fixed_size: 29696
    .kernarg_segment_align: 8
    .kernarg_segment_size: 184
    .language:       OpenCL C
    .language_version:
      - 2
      - 0
    .max_flat_workgroup_size: 512
    .name:           _Z12front_kernelPKiS0_PKfS2_S2_S2_S2_S2_S2_S2_S2_S2_S2_PjS3_PiS4_PDF16_PfS6_S4_S5_S0_
    .private_segment_fixed_size: 0
    .sgpr_count:     30
    .sgpr_spill_count: 0
    .symbol:         _Z12front_kernelPKiS0_PKfS2_S2_S2_S2_S2_S2_S2_S2_S2_S2_PjS3_PiS4_PDF16_PfS6_S4_S5_S0_.kd
    .uniform_work_group_size: 1
    .uses_dynamic_stack: false
    .vgpr_count:     80
    .vgpr_spill_count: 0
    .wavefront_size: 64
  - .agpr_count:     0
    .args:
      - .actual_access:  read_only
        .address_space:  global
        .offset:         0
        .size:           8
        .value_kind:     global_buffer
      - .actual_access:  read_only
        .address_space:  global
        .offset:         8
        .size:           8
        .value_kind:     global_buffer
      - .actual_access:  write_only
        .address_space:  global
        .offset:         16
        .size:           8
        .value_kind:     global_buffer
      - .actual_access:  write_only
        .address_space:  global
        .offset:         24
        .size:           8
        .value_kind:     global_buffer
      - .actual_access:  write_only
        .address_space:  global
        .offset:         32
        .size:           8
        .value_kind:     global_buffer
      - .actual_access:  read_only
        .address_space:  global
        .offset:         40
        .size:           8
        .value_kind:     global_buffer
      - .actual_access:  read_only
        .address_space:  global
        .offset:         48
        .size:           8
        .value_kind:     global_buffer
      - .actual_access:  write_only
        .address_space:  global
        .offset:         56
        .size:           8
        .value_kind:     global_buffer
      - .actual_access:  write_only
        .address_space:  global
        .offset:         64
        .size:           8
        .value_kind:     global_buffer
    .group_segment_fixed_size: 40960
    .kernarg_segment_align: 8
    .kernarg_segment_size: 72
    .language:       OpenCL C
    .language_version:
      - 2
      - 0
    .max_flat_workgroup_size: 512
    .name:           _Z13second_kernelPKfPKDF16_PDF16_PfS4_PKjPKiPiS9_
    .private_segment_fixed_size: 0
    .sgpr_count:     34
    .sgpr_spill_count: 0
    .symbol:         _Z13second_kernelPKfPKDF16_PDF16_PfS4_PKjPKiPiS9_.kd
    .uniform_work_group_size: 1
    .uses_dynamic_stack: false
    .vgpr_count:     64
    .vgpr_spill_count: 0
    .wavefront_size: 64
  - .agpr_count:     0
    .args:
      - .actual_access:  read_only
        .address_space:  global
        .offset:         0
        .size:           8
        .value_kind:     global_buffer
      - .actual_access:  read_only
        .address_space:  global
        .offset:         8
        .size:           8
        .value_kind:     global_buffer
      - .actual_access:  read_only
        .address_space:  global
        .offset:         16
        .size:           8
        .value_kind:     global_buffer
      - .actual_access:  read_only
        .address_space:  global
        .offset:         24
        .size:           8
        .value_kind:     global_buffer
      - .actual_access:  read_only
        .address_space:  global
        .offset:         32
        .size:           8
        .value_kind:     global_buffer
      - .actual_access:  read_only
        .address_space:  global
        .offset:         40
        .size:           8
        .value_kind:     global_buffer
      - .actual_access:  read_only
        .address_space:  global
        .offset:         48
        .size:           8
        .value_kind:     global_buffer
      - .actual_access:  write_only
        .address_space:  global
        .offset:         56
        .size:           8
        .value_kind:     global_buffer
      - .actual_access:  write_only
        .address_space:  global
        .offset:         64
        .size:           8
        .value_kind:     global_buffer
      - .actual_access:  write_only
        .address_space:  global
        .offset:         72
        .size:           8
        .value_kind:     global_buffer
      - .offset:         80
        .size:           4
        .value_kind:     by_value
    .group_segment_fixed_size: 10768
    .kernarg_segment_align: 8
    .kernarg_segment_size: 84
    .language:       OpenCL C
    .language_version:
      - 2
      - 0
    .max_flat_workgroup_size: 256
    .name:           _Z11agg1_kernelPKDF16_PKfS2_PKiS4_S2_S2_PDF16_PfS6_i
    .private_segment_fixed_size: 0
    .sgpr_count:     54
    .sgpr_spill_count: 0
    .symbol:         _Z11agg1_kernelPKDF16_PKfS2_PKiS4_S2_S2_PDF16_PfS6_i.kd
    .uniform_work_group_size: 1
    .uses_dynamic_stack: false
    .vgpr_count:     70
    .vgpr_spill_count: 0
    .wavefront_size: 64
  - .agpr_count:     0
    .args:
      - .actual_access:  read_only
        .address_space:  global
        .offset:         0
        .size:           8
        .value_kind:     global_buffer
      - .actual_access:  read_only
        .address_space:  global
        .offset:         8
        .size:           8
        .value_kind:     global_buffer
      - .actual_access:  read_only
        .address_space:  global
        .offset:         16
        .size:           8
        .value_kind:     global_buffer
      - .actual_access:  read_only
        .address_space:  global
        .offset:         24
        .size:           8
        .value_kind:     global_buffer
      - .actual_access:  read_only
        .address_space:  global
        .offset:         32
        .size:           8
        .value_kind:     global_buffer
      - .actual_access:  write_only
        .address_space:  global
        .offset:         40
        .size:           8
        .value_kind:     global_buffer
      - .offset:         48
        .size:           4
        .value_kind:     by_value
    .group_segment_fixed_size: 0
    .kernarg_segment_align: 8
    .kernarg_segment_size: 52
    .language:       OpenCL C
    .language_version:
      - 2
      - 0
    .max_flat_workgroup_size: 256
    .name:           _Z13stats2_kernelPKiS0_PKfS2_S0_P15HIP_vector_typeIfLj4EEi
    .private_segment_fixed_size: 0
    .sgpr_count:     38
    .sgpr_spill_count: 0
    .symbol:         _Z13stats2_kernelPKiS0_PKfS2_S0_P15HIP_vector_typeIfLj4EEi.kd
    .uniform_work_group_size: 1
    .uses_dynamic_stack: false
    .vgpr_count:     32
    .vgpr_spill_count: 0
    .wavefront_size: 64
  - .agpr_count:     0
    .args:
      - .actual_access:  read_only
        .address_space:  global
        .offset:         0
        .size:           8
        .value_kind:     global_buffer
      - .actual_access:  read_only
        .address_space:  global
        .offset:         8
        .size:           8
        .value_kind:     global_buffer
      - .actual_access:  read_only
        .address_space:  global
        .offset:         16
        .size:           8
        .value_kind:     global_buffer
      - .actual_access:  read_only
        .address_space:  global
        .offset:         24
        .size:           8
        .value_kind:     global_buffer
      - .actual_access:  read_only
        .address_space:  global
        .offset:         32
        .size:           8
        .value_kind:     global_buffer
      - .actual_access:  write_only
        .address_space:  global
        .offset:         40
        .size:           8
        .value_kind:     global_buffer
      - .offset:         48
        .size:           4
        .value_kind:     by_value
    .group_segment_fixed_size: 70752
    .kernarg_segment_align: 8
    .kernarg_segment_size: 52
    .language:       OpenCL C
    .language_version:
      - 2
      - 0
    .max_flat_workgroup_size: 1024
    .name:           _Z12pool2_kernelPKjPKiPKfPK15HIP_vector_typeIfLj4EEPKDF16_Pfi
    .private_segment_fixed_size: 0
    .sgpr_count:     26
    .sgpr_spill_count: 0
    .symbol:         _Z12pool2_kernelPKjPKiPKfPK15HIP_vector_typeIfLj4EEPKDF16_Pfi.kd
    .uniform_work_group_size: 1
    .uses_dynamic_stack: false
    .vgpr_count:     128
    .vgpr_spill_count: 0
    .wavefront_size: 64
  - .agpr_count:     0
    .args:
      - .actual_access:  read_only
        .address_space:  global
        .offset:         0
        .size:           8
        .value_kind:     global_buffer
      - .actual_access:  read_only
        .address_space:  global
        .offset:         8
        .size:           8
        .value_kind:     global_buffer
      - .actual_access:  read_only
        .address_space:  global
        .offset:         16
        .size:           8
        .value_kind:     global_buffer
      - .actual_access:  read_only
        .address_space:  global
        .offset:         24
        .size:           8
        .value_kind:     global_buffer
      - .actual_access:  read_only
        .address_space:  global
        .offset:         32
        .size:           8
        .value_kind:     global_buffer
      - .actual_access:  read_only
        .address_space:  global
        .offset:         40
        .size:           8
        .value_kind:     global_buffer
      - .actual_access:  read_only
        .address_space:  global
        .offset:         48
        .size:           8
        .value_kind:     global_buffer
      - .actual_access:  read_only
        .address_space:  global
        .offset:         56
        .size:           8
        .value_kind:     global_buffer
      - .actual_access:  write_only
        .address_space:  global
        .offset:         64
        .size:           8
        .value_kind:     global_buffer
    .group_segment_fixed_size: 9472
    .kernarg_segment_align: 8
    .kernarg_segment_size: 72
    .language:       OpenCL C
    .language_version:
      - 2
      - 0
    .max_flat_workgroup_size: 1024
    .name:           _Z10mlp_kernelPKfPKiS0_S0_S0_S0_S0_S0_Pf
    .private_segment_fixed_size: 0
    .sgpr_count:     76
    .sgpr_spill_count: 0
    .symbol:         _Z10mlp_kernelPKfPKiS0_S0_S0_S0_S0_S0_Pf.kd
    .uniform_work_group_size: 1
    .uses_dynamic_stack: false
    .vgpr_count:     77
    .vgpr_spill_count: 0
    .wavefront_size: 64
